# speedup vs baseline: 1.1728x; 1.0313x over previous
.Lco_nopoll:
	s_waitcnt lgkmcnt(0)
	s_barrier
	v_mov_b32_e32 v76, 0
	v_mov_b32_e32 v77, 0
	v_mov_b32_e32 v78, 0
	v_mov_b32_e32 v79, 0
	ds_write_b128 v74, v[76:79]
	ds_write_b128 v74, v[76:79] offset:8192
	ds_write_b128 v74, v[76:79] offset:16384
	ds_write_b128 v74, v[76:79] offset:24576
	ds_write_b128 v74, v[76:79] offset:32768
	ds_write_b128 v74, v[76:79] offset:40960
	ds_write_b128 v74, v[76:79] offset:49152
	ds_write_b128 v74, v[76:79] offset:57344
	v_mov_b32_e32 v0, 0x26400
	v_lshl_add_u32 v0, v75, 5, v0
	ds_read_b128 v[36:39], v0
	ds_read_b128 v[40:43], v0 offset:16
	s_waitcnt lgkmcnt(0)
	v_or3_b32 v44, v36, v37, v38
	v_or3_b32 v44, v44, v39, v40
	v_or3_b32 v44, v44, v41, v42
	v_or_b32_e32 v44, v44, v43
	v_bfe_u32 v44, v44, 15, 1
	v_and_b32_e32 v36, 0x7f, v36
	v_and_b32_e32 v37, 0x7f, v37
	v_and_b32_e32 v38, 0x7f, v38
	v_and_b32_e32 v39, 0x7f, v39
	v_and_b32_e32 v40, 0x7f, v40
	v_and_b32_e32 v41, 0x7f, v41
	v_and_b32_e32 v42, 0x7f, v42
	v_and_b32_e32 v43, 0x7f, v43
	v_mov_b32_e32 v45, v36
	v_add_u32_e32 v46, v45, v37
	v_add_u32_e32 v47, v46, v38
	v_add_u32_e32 v48, v47, v39
	v_add_u32_e32 v49, v48, v40
	v_add_u32_e32 v50, v49, v41
	v_add_u32_e32 v51, v50, v42
	v_add_u32_e32 v52, v51, v43
	v_cmp_lt_u32_e32 vcc, 0x100, v52
	v_add_u32_e32 v53, 15, v52
	v_lshrrev_b32_e32 v53, 4, v53
	v_cndmask_b32_e64 v54, 0, 1, vcc
	v_or_b32_e32 v44, v44, v54
	v_mov_b32_e32 v55, 0x26c00
	ds_max_u32 v55, v53
	ds_or_b32 v55, v44 offset:4
	s_waitcnt lgkmcnt(0)
	s_barrier
	ds_read_b64 v[0:1], v55
	v_lshlrev_b32_e32 v56, 5, v45
	v_lshlrev_b32_e32 v57, 5, v46
	v_lshlrev_b32_e32 v58, 5, v47
	v_lshlrev_b32_e32 v59, 5, v48
	v_lshlrev_b32_e32 v60, 5, v49
	v_lshlrev_b32_e32 v61, 5, v50
	v_lshlrev_b32_e32 v62, 5, v51
	v_sub_u32_e32 v56, 0x800, v56
	v_sub_u32_e32 v57, 0x1000, v57
	v_sub_u32_e32 v58, 0x1800, v58
	v_sub_u32_e32 v59, 0x2000, v59
	v_sub_u32_e32 v60, 0x2800, v60
	v_sub_u32_e32 v61, 0x3000, v61
	v_sub_u32_e32 v62, 0x3800, v62
	v_add_u32_e32 v63, s3, v75
	v_lshlrev_b32_e32 v63, 14, v63
	v_add_u32_e32 v63, 0x800000, v63
	s_waitcnt lgkmcnt(0)
	v_readfirstlane_b32 s77, v0
	v_readfirstlane_b32 s36, v1
	s_cmp_lg_u32 s36, 0
	s_cselect_b64 s[6:7], 0, -1
	s_cmp_gt_u32 s10, 3
	s_cbranch_scc1 .Lco_done
	s_cmp_lg_u32 s36, 0
	s_cbranch_scc1 .Lco_gen
	v_mov_b32_e32 v0, v70
	v_cmp_lt_u32_e64 s[12:13], v0, v52
	v_cmp_le_u32_e64 s[16:17], v45, v0
	v_cmp_le_u32_e64 s[18:19], v46, v0
	v_cmp_le_u32_e64 s[20:21], v47, v0
	v_cmp_le_u32_e64 s[22:23], v48, v0
	v_cmp_le_u32_e64 s[24:25], v49, v0
	v_cmp_le_u32_e64 s[26:27], v50, v0
	v_cmp_le_u32_e64 s[28:29], v51, v0
	v_cndmask_b32_e64 v1, 0, v56, s[16:17]
	v_cndmask_b32_e64 v1, v1, v57, s[18:19]
	v_cndmask_b32_e64 v1, v1, v58, s[20:21]
	v_cndmask_b32_e64 v1, v1, v59, s[22:23]
	v_cndmask_b32_e64 v1, v1, v60, s[24:25]
	v_cndmask_b32_e64 v1, v1, v61, s[26:27]
	v_cndmask_b32_e64 v1, v1, v62, s[28:29]
	v_lshl_add_u32 v2, v0, 5, v63
	v_add_u32_e32 v2, v2, v1
	s_and_saveexec_b64 s[30:31], s[12:13]
	s_cbranch_execz .Lco_nold0
	global_load_dwordx4 v[208:211], v2, s[66:67] sc1
	global_load_dword v71, v2, s[66:67] offset:16 sc1
	v_mov_b32_e32 v18, 1.0

.Lk_267:
	s_or_b64 exec, exec, s[44:45]
	s_waitcnt lgkmcnt(1)
	v_mov_b32_e32 v0, s56
	v_mov_b32_e32 v1, s57
	v_or_b32_e32 v6, s3, v75
	s_lshl_b32 s24, s75, 9
	v_mov_b32_e32 v7, v34
	v_mov_b32_e32 v2, s58
	v_mov_b32_e32 v3, s59
	v_add_u32_e32 v4, s24, v6
	v_mov_b32_e32 v5, v34
	v_lshl_add_u64 v[0:1], v[6:7], 2, v[0:1]
	v_and_b32_e32 v160, 0xff, v98
	v_lshl_add_u64 v[2:3], v[4:5], 2, v[2:3]
	v_mov_b32_e32 v5, v252
	v_lshlrev_b32_e32 v0, 2, v160
	v_mov_b32_e32 v4, v253
	s_mov_b32 s69, s68
	s_mov_b32 s70, s68
	s_mov_b32 s71, s68
	v_mov_b64_e32 v[10:11], s[68:69]
	v_or_b32_e32 v0, 0xc00, v98
	s_movk_i32 s0, 0xe00
	s_getreg_b32 s11, hwreg(HW_REG_XCC_ID, 0, 4)
	v_mov_b64_e32 v[12:13], s[70:71]
	v_cmp_gt_u32_e32 vcc, s0, v0
	s_lshr_b32 s10, s76, 6
	s_add_u32 s14, s66, 0x400000
	s_addc_u32 s15, s67, 0
	s_and_saveexec_b64 s[0:1], s[42:43]
	s_xor_b64 s[0:1], exec, s[0:1]
	s_lshl_b32 s12, s10, 2
	s_or_saveexec_b64 s[0:1], s[0:1]
	v_mov_b32_e32 v2, 0
	s_and_b32 s68, s11, 15
	v_mov_b32_e32 v3, v2
	v_mov_b32_e32 v163, s12
	s_xor_b64 exec, exec, s[0:1]
	s_cbranch_execz .Lk_283
	v_mov_b32_e32 v0, 0x24400
	v_lshl_or_b32 v0, v75, 2, v0
	ds_read_b32 v3, v0
	s_waitcnt vmcnt(2)
	v_cvt_f64_f32_e32 v[0:1], v4
	s_lshl_b32 s20, s10, 2
	s_waitcnt lgkmcnt(0)
	v_cvt_f64_f32_e32 v[6:7], v3
	v_add_f64 v[0:1], v[0:1], v[6:7]
	v_cmp_le_f64_e64 s[16:17], 1.0, v[0:1]
	s_lshr_b32 s18, s16, 15
	s_lshr_b64 s[12:13], s[16:17], 30
	s_and_b32 s11, s16, 1
	s_and_b32 s13, s18, 2
	s_and_b32 s12, s12, 4
	s_or_b32 s11, s13, s11
	s_or_b32 s11, s11, s12
	s_lshr_b32 s12, s17, 13
	s_and_b32 s12, s12, 8
	s_or_b32 s11, s11, s12
	s_lshl_b32 s21, s11, s20
	s_and_saveexec_b64 s[10:11], s[4:5]
	s_cbranch_execz .Lk_276
	s_mov_b64 s[18:19], exec
	v_mbcnt_lo_u32_b32 v2, s18, 0
	v_mbcnt_hi_u32_b32 v2, s19, v2
	s_or_b32 s22, s21, 0x10000
	v_cmp_eq_u32_e32 vcc, 0, v2
	s_and_saveexec_b64 s[12:13], vcc
	s_bcnt1_i32_b64 s18, s[18:19]
	s_mul_i32 s18, s22, s18
	v_mov_b32_e32 v3, 0x26c10
	v_mov_b32_e32 v4, s18
	ds_add_rtn_u32 v3, v3, v4
	s_or_b64 exec, exec, s[12:13]
	s_waitcnt lgkmcnt(0)
	v_readfirstlane_b32 s12, v3
	v_mul_lo_u32 v2, s22, v2
	s_nop 0
	v_add_u32_e32 v2, s12, v2

.Lk_283:
	s_or_b64 exec, exec, s[0:1]
	v_lshrrev_b32_e32 v4, 4, v160
	s_lshl_b32 s0, s78, 5
	v_or_b32_e32 v165, s0, v4
	v_mov_b32_e32 v4, 0x24400
	s_add_i32 s69, s33, 33
	v_lshl_or_b32 v169, v72, 2, v4
	v_mul_u32_u24_e32 v4, 10, v160
	s_cmp_gt_i32 s77, 8
	s_cselect_b64 s[18:19], -1, 0
	s_cmp_gt_i32 s77, 10
	v_lshlrev_b32_e32 v12, 2, v4
	v_mov_b32_e32 v13, 0
	v_or_b32_e32 v164, 0x100, v160
	v_cvt_f64_f32_e32 v[10:11], v5
	v_mov_b32_e32 v5, 0x10000
	s_cselect_b64 s[20:21], -1, 0
	s_cmp_gt_i32 s77, 12
	v_lshl_add_u64 v[14:15], s[48:49], 0, v[12:13]
	v_lshlrev_b32_e32 v4, 9, v70
	v_lshlrev_b32_e32 v12, 2, v70
	v_lshl_or_b32 v67, v160, 2, v5
	v_lshl_or_b32 v69, v164, 2, v5
	s_cselect_b64 s[22:23], -1, 0
	v_add3_u32 v172, v4, s3, v75
	v_lshl_add_u64 v[4:5], s[60:61], 0, v[12:13]
	s_add_i32 s24, s24, s3
	v_lshl_add_u64 v[40:41], v[4:5], 0, 64
	v_add_u32_e32 v4, s24, v75
	v_mov_b32_e32 v5, v13
	v_lshlrev_b64 v[4:5], 11, v[4:5]
	v_cmp_gt_f32_e32 vcc, 0, v161
	v_or_b32_e32 v4, v4, v12
	v_lshrrev_b32_e32 v6, 4, v164
	v_cndmask_b32_e64 v167, 0, 1.0, vcc
	v_cmp_gt_f32_e32 vcc, 0, v162
	s_mov_b64 s[10:11], 0x2800
	s_lshl_b32 s70, s68, 16
	v_lshl_add_u64 v[4:5], s[72:73], 0, v[4:5]
	v_mov_b32_e32 v12, v13
	s_mov_b32 s26, 0x3f7d73e7
	s_mov_b32 s28, 0xa37fcc69
	s_mov_b32 s34, 0x3f779b79
	s_mov_b32 s36, 0x3d064869
	v_or_b32_e32 v166, s0, v6
	v_cndmask_b32_e64 v168, 0, 1.0, vcc
	v_cmp_gt_u32_e64 s[0:1], 32, v73
	v_lshl_add_u32 v170, v73, 5, s33
	v_lshl_add_u64 v[34:35], v[14:15], 0, s[10:11]
	s_bitset1_b32 s70, 21
	v_lshlrev_b32_e32 v171, 3, v70
	v_lshl_add_u64 v[42:43], v[4:5], 0, 64
	s_mov_b64 s[38:39], 0
	v_mov_b64_e32 v[44:45], 0
	s_mov_b64 s[24:25], 0
	s_mov_b32 s27, 0x3d8414e8
	s_mov_b32 s29, 0x3fee7078
	s_mov_b32 s3, 0xf000
	s_mov_b64 s[30:31], 0x80
	s_mov_b32 s35, 0x3f7383c5
	s_mov_b32 s37, 0x3d47c3ae
	s_mov_b32 s71, 0xffff
	v_mov_b32_e32 v47, 0x3f6f7d63
	v_bfrev_b32_e32 v173, 1
	v_mov_b32_e32 v174, 0x2f0
	v_mov_b32_e32 v175, 0x26c10
	s_mov_b64 s[40:41], 0
	s_mov_b64 s[44:45], 0
	v_mov_b32_e32 v176, 0
	v_mov_b64_e32 v[36:37], 0
	v_mov_b64_e32 v[6:7], 0
	v_mov_b64_e32 v[48:49], 0
	v_mov_b64_e32 v[38:39], 0
	v_mov_b64_e32 v[4:5], 0
	v_mov_b32_e32 v177, 0
	v_mov_b64_e32 v[50:51], v[12:13]
	v_mov_b64_e32 v[56:57], v[12:13]
	v_mov_b64_e32 v[52:53], v[12:13]
	v_mov_b64_e32 v[58:59], v[12:13]
	v_mov_b32_e32 v54, v13
	v_mov_b32_e32 v55, v13
	v_mul_f32_e32 v218, v9, v18
	v_mul_f32_e32 v219, v131, v19
	v_mul_f32_e32 v220, v134, v20
	v_mul_f32_e32 v221, v137, v21
	v_mul_f32_e32 v222, v140, v22
	v_mul_f32_e32 v223, v143, v23
	v_mul_f32_e32 v224, v146, v24
	v_mul_f32_e32 v225, v150, v25
	v_mul_f32_e32 v226, v121, v26
	v_mul_f32_e32 v227, v122, v27
	v_mov_b32_e32 v250, 0
	v_add_u16_e32 v208, v250, v159
	v_add_u16_e32 v209, v250, v158
	v_add_u16_e32 v210, v250, v157
	v_add_u16_e32 v211, v250, v156
	v_add_u16_e32 v212, v250, v155
	v_add_u16_e32 v213, v250, v154
	v_add_u16_e32 v214, v250, v153
	v_add_u16_e32 v215, v250, v149
	v_add_u16_e32 v216, v250, v128
	v_add_u16_e32 v217, v250, v127
	s_mov_b64 s[86:87], 0
	s_and_saveexec_b64 s[82:83], s[42:43]
	v_lshlrev_b32_e32 v208, 2, v165
	v_lshlrev_b32_e32 v210, 2, v166
	v_add_u32_e32 v208, 0x400000, v208
	v_add_u32_e32 v210, 0x400000, v210
	v_mov_b32_e32 v209, 0x8000
	v_mov_b32_e32 v211, 0x8000
	s_mov_b64 exec, s[82:83]
	s_branch .Lk_288

.Lk_293:
	s_or_b64 exec, exec, s[12:13]
	v_add_f32_e32 v216, 1.0, v52
	v_add_f32_e32 v217, 1.0, v50
	v_lshlrev_b32_e32 v215, 9, v177
	v_cmp_neq_f32_e32 vcc, 0, v216
	v_and_b32_e32 v215, 0x1e00, v215
	v_or_b32_e32 v250, v215, v160
	v_cndmask_b32_e32 v216, v173, v216, vcc
	v_cmp_neq_f32_e32 vcc, 0, v217
	v_or_b32_e32 v251, v215, v164
	v_lshlrev_b32_e32 v250, 3, v250
	v_cndmask_b32_e32 v217, v173, v217, vcc
	v_lshlrev_b32_e32 v251, 3, v251
	s_waitcnt vmcnt(0)
	v_mov_b32_e32 v64, v182
	v_mov_b32_e32 v46, v183
	s_xor_b64 s[50:51], s[44:45], -1
	v_add_u32_e32 v12, 1, v177
	s_mov_b64 s[12:13], -1
	s_and_saveexec_b64 s[48:49], s[50:51]
	s_cbranch_execz .Lk_303
	v_lshrrev_b32_e32 v65, 20, v64
	v_cmp_eq_u32_e32 vcc, v65, v12
	v_lshrrev_b32_e32 v65, 20, v46
	v_cmp_eq_u32_e64 s[12:13], v65, v12
	s_and_b64 s[12:13], vcc, s[12:13]
	s_nop 0
	v_cndmask_b32_e64 v65, 0, 1, s[12:13]
	v_cmp_ne_u32_e32 vcc, 0, v65
	s_cmp_eq_u64 vcc, exec
	s_mov_b64 s[12:13], 0
	s_cbranch_scc1 .Lk_302
	v_lshlrev_b32_e32 v72, 13, v177
	v_and_b32_e32 v72, 0x6000, v72
	v_add_u32_e32 v65, v72, v166
	v_add_u32_e32 v72, v72, v165
	v_mov_b32_e32 v73, 0
	v_lshlrev_b64 v[56:57], 7, v[72:73]
	v_mov_b32_e32 v72, v65
	v_lshl_add_u64 v[56:57], s[66:67], 0, v[56:57]
	v_lshlrev_b64 v[60:61], 7, v[72:73]
	v_mov_b32_e32 v72, v213
	v_lshl_add_u64 v[60:61], s[66:67], 0, v[60:61]
	v_lshl_add_u64 v[58:59], s[66:67], 0, v[72:73]
	v_mov_b32_e32 v72, v214
	s_nop 0
	v_lshl_add_u64 v[62:63], s[66:67], 0, v[72:73]
	s_cmp_eq_u64 s[10:11], 0
	s_cselect_b32 s89, 0xff, 3
	s_mov_b32 s60, 0
.Lk_296:
	s_cmp_gt_u32 s60, s89
	s_cselect_b64 s[12:13], -1, 0
	s_bitcmp1_b32 s60, 0
	s_cselect_b64 s[50:51], -1, 0
	v_lshrrev_b32_e32 v65, 20, v64
	s_and_b64 vcc, s[12:13], s[50:51]
	v_cmp_ne_u32_e64 s[12:13], v65, v12
	s_and_saveexec_b64 s[50:51], s[12:13]
	s_cbranch_execz .Lk_298
	v_cndmask_b32_e32 v65, v59, v57, vcc
	v_cndmask_b32_e32 v64, v58, v56, vcc
	global_load_dword v64, v[64:65], off sc1

.Lk_303:
	s_or_b64 exec, exec, s[48:49]
	v_lshrrev_b32_e32 v57, v70, v64
	v_lshrrev_b32_e32 v65, v70, v46
	v_bfe_i32 v60, v57, 0, 1
	v_bfe_i32 v62, v65, 0, 1
	v_and_b32_e32 v60, v60, v216
	v_and_b32_e32 v62, v62, v217
	ds_write2_b32 v250, v60, v53 offset1:1
	ds_write2_b32 v251, v62, v51 offset1:1
	v_and_b32_e32 v59, 1, v57
	v_and_b32_e32 v57, 1, v65
	v_cvt_f32_ubyte0_e32 v59, v59
	v_cvt_f32_ubyte0_e32 v57, v57
	v_mov_b32_e32 v56, v50
	v_mov_b32_e32 v58, v52
	s_cmp_eq_u64 s[10:11], 0
	s_cbranch_scc1 .Lmy_rx_nt0
	v_bfe_u32 v60, v46, 16, 4
	v_bfe_u32 v61, v64, 16, 4
	v_cmp_eq_u32_e64 s[48:49], s68, v60
	v_cmp_eq_u32_e64 s[50:51], s68, v61
	v_lshlrev_b32_e32 v60, 2, v165
	v_lshlrev_b32_e32 v61, 2, v166
	v_add_u32_e32 v60, 0x400000, v60
	v_add_u32_e32 v61, 0x400000, v61
	v_lshlrev_b32_e32 v62, 7, v165
	v_lshlrev_b32_e32 v63, 7, v166
	v_cndmask_b32_e64 v208, v62, v60, s[50:51]
	v_cndmask_b32_e64 v210, v63, v61, s[48:49]
	v_mov_b32_e32 v60, 0x8000
	v_mov_b32_e32 v62, 0x100000
	v_cndmask_b32_e64 v209, v62, v60, s[50:51]
	v_cndmask_b32_e64 v211, v62, v60, s[48:49]
	s_branch .Lmy_rx_end
